# v69 + window branch boundary tiles: per-element clamp/compare/select masking on per-lane bounds instead of SGPR-pair masks spilled through lanes
# speedup vs baseline: 1.0024x; 1.0024x over previous
; #define LAS __attribute__((address_space(3)))
; __device__ __forceinline__ void attn_qk2z(LAS unsigned char* Kb, const bf16x8 (&q)[2][2], int fr, int g4, f32x4 (&s)[2][4]) {
;     bf16x8 kf[4][2];
; #pragma unroll
;     for (int c = 0; c < 4; ++c)
; #pragma unroll
;         for (int ks = 0; ks < 2; ++ks) kf[c][ks] = *(const LAS bf16x8*)(Kb + pg8::lds_byte(16 * c + fr, 32 * ks + 8 * g4));
;     __builtin_amdgcn_sched_barrier(0);
; #pragma unroll
;     for (int c = 0; c < 4; ++c) {
; #pragma unroll
;         for (int ks = 0; ks < 2; ++ks) {
; #pragma unroll
;             for (int rb = 0; rb < 2; ++rb) s[rb][c] = __builtin_amdgcn_mfma_f32_16x16x32_bf16(kf[c][ks], q[rb][ks], ks == 0 ? (f32x4){0.f, 0.f, 0.f, 0.f} : s[rb][c], 0, 0, 0);
;         }
;     }
; }
; __device__ __forceinline__ void attn_step2x_nomax(LAS unsigned char* Vb, f32x4 (&s)[2][4], AttnRow (&st)[2], int kbase, int g4, const int (&lo)[2], const int (&hi)[2], const unsigned (&enm)[2], bool emask,
;                                                   int vlane, int swz, const bf16x8 onesf) {
;     if (emask) {
; #pragma unroll
;         for (int rb = 0; rb < 2; ++rb)
; #pragma unroll
;             for (int c = 0; c < 4; ++c)
; #pragma unroll
;                 for (int i = 0; i < 4; ++i) { const int key = kbase + 16 * c + 4 * g4 + i; if (key < lo[rb] || key > hi[rb]) s[rb][c][i] = -INFINITY; }
;     }
.LBB0_2161:
	v_add_u32_e32 v110, s24, v220
	ds_read_b128 v[66:69], v110
	ds_read_b128 v[70:73], v110 offset:1024
	ds_read_b128 v[78:81], v110 offset:2048
	ds_read_b128 v[82:85], v110 offset:3072
	ds_read_b128 v[86:89], v110 offset:4096
	ds_read_b128 v[98:101], v110 offset:5120
	ds_read_b128 v[102:105], v110 offset:6144
	ds_read_b128 v[112:115], v110 offset:7168
	v_readlane_b32 s0, v251, 13
	s_cmp_eq_u32 s0, s33
	v_readlane_b32 s4, v251, 11
	v_readlane_b32 s6, v251, 14
	s_cselect_b64 s[0:1], -1, 0
	s_cmp_lt_i32 s6, s4
	s_cselect_b64 s[4:5], -1, 0
	s_or_b64 s[0:1], s[0:1], s[4:5]
	s_waitcnt lgkmcnt(0)
	v_mfma_f32_16x16x32_bf16 v[74:77], v[66:69], v[10:13], 0
	s_andn2_b64 vcc, exec, s[0:1]
	v_mfma_f32_16x16x32_bf16 v[66:69], v[66:69], v[18:21], 0
	v_mfma_f32_16x16x32_bf16 v[94:97], v[70:73], v[14:17], v[74:77]
	v_mfma_f32_16x16x32_bf16 v[74:77], v[70:73], v[22:25], v[66:69]
	v_mfma_f32_16x16x32_bf16 v[66:69], v[78:81], v[10:13], 0
	v_mfma_f32_16x16x32_bf16 v[70:73], v[78:81], v[18:21], 0
	v_mfma_f32_16x16x32_bf16 v[90:93], v[82:85], v[14:17], v[66:69]
	v_mfma_f32_16x16x32_bf16 v[66:69], v[86:89], v[10:13], 0
	v_mfma_f32_16x16x32_bf16 v[78:81], v[86:89], v[18:21], 0
	v_mfma_f32_16x16x32_bf16 v[86:89], v[98:101], v[14:17], v[66:69]
	v_mfma_f32_16x16x32_bf16 v[66:69], v[98:101], v[22:25], v[78:81]
	v_mfma_f32_16x16x32_bf16 v[78:81], v[102:105], v[10:13], 0
	v_mfma_f32_16x16x32_bf16 v[98:101], v[102:105], v[18:21], 0
	v_mfma_f32_16x16x32_bf16 v[70:73], v[82:85], v[22:25], v[70:73]
	v_mfma_f32_16x16x32_bf16 v[82:85], v[112:115], v[14:17], v[78:81]
	v_mfma_f32_16x16x32_bf16 v[78:81], v[112:115], v[22:25], v[98:101]
	s_cbranch_vccnz .LBB0_2165
	s_nop 2
	v_add_u32_e32 v2, s6, v138
	v_sub_u32_e32 v4, v1, v2
	v_sub_u32_e32 v5, v106, v2
	v_sub_u32_e32 v98, v107, v2
	v_sub_u32_e32 v99, v108, v2
	v_med3_i32 v100, 0, v98, v99
	v_med3_i32 v101, 0, v4, v5
	v_med3_i32 v102, 1, v98, v99
	v_cmp_ne_u32_e64 s[0:1], 0, v100
	v_cmp_ne_u32_e64 s[4:5], 0, v101
	v_cmp_ne_u32_e64 s[8:9], 1, v102
	v_cndmask_b32_e64 v94, v94, v246, s[0:1]
	v_cndmask_b32_e64 v74, v74, v246, s[4:5]
	v_cndmask_b32_e64 v95, v95, v246, s[8:9]
	v_med3_i32 v100, 1, v4, v5
	v_med3_i32 v101, 2, v98, v99
	v_med3_i32 v102, 2, v4, v5
	v_cmp_ne_u32_e64 s[0:1], 1, v100
	v_cmp_ne_u32_e64 s[4:5], 2, v101
	v_cmp_ne_u32_e64 s[8:9], 2, v102
	v_cndmask_b32_e64 v75, v75, v246, s[0:1]
	v_cndmask_b32_e64 v96, v96, v246, s[4:5]
	v_cndmask_b32_e64 v76, v76, v246, s[8:9]
	v_med3_i32 v100, 3, v98, v99
	v_med3_i32 v101, 3, v4, v5
	v_med3_i32 v102, 16, v98, v99
	v_cmp_ne_u32_e64 s[0:1], 3, v100
	v_cmp_ne_u32_e64 s[4:5], 3, v101
	v_cmp_ne_u32_e64 s[8:9], 16, v102
	v_cndmask_b32_e64 v97, v97, v246, s[0:1]
	v_cndmask_b32_e64 v77, v77, v246, s[4:5]
	v_cndmask_b32_e64 v90, v90, v246, s[8:9]
	v_med3_i32 v100, 16, v4, v5
	v_med3_i32 v101, 17, v98, v99
	v_med3_i32 v102, 17, v4, v5
	v_cmp_ne_u32_e64 s[0:1], 16, v100
	v_cmp_ne_u32_e64 s[4:5], 17, v101
	v_cmp_ne_u32_e64 s[8:9], 17, v102
	v_cndmask_b32_e64 v70, v70, v246, s[0:1]
	v_cndmask_b32_e64 v91, v91, v246, s[4:5]
	v_cndmask_b32_e64 v71, v71, v246, s[8:9]
	v_med3_i32 v100, 18, v98, v99
	v_med3_i32 v101, 18, v4, v5
	v_med3_i32 v102, 19, v98, v99
	v_cmp_ne_u32_e64 s[0:1], 18, v100
	v_cmp_ne_u32_e64 s[4:5], 18, v101
	v_cmp_ne_u32_e64 s[8:9], 19, v102
	v_cndmask_b32_e64 v92, v92, v246, s[0:1]
	v_cndmask_b32_e64 v72, v72, v246, s[4:5]
	v_cndmask_b32_e64 v93, v93, v246, s[8:9]
	v_med3_i32 v100, 19, v4, v5
	v_med3_i32 v101, 32, v98, v99
	v_med3_i32 v102, 32, v4, v5
	v_cmp_ne_u32_e64 s[0:1], 19, v100
	v_cmp_ne_u32_e64 s[4:5], 32, v101
	v_cmp_ne_u32_e64 s[8:9], 32, v102
	v_cndmask_b32_e64 v73, v73, v246, s[0:1]
	v_cndmask_b32_e64 v86, v86, v246, s[4:5]
	v_cndmask_b32_e64 v66, v66, v246, s[8:9]
	v_med3_i32 v100, 33, v98, v99
	v_med3_i32 v101, 33, v4, v5
	v_med3_i32 v102, 34, v98, v99
	v_cmp_ne_u32_e64 s[0:1], 33, v100
	v_cmp_ne_u32_e64 s[4:5], 33, v101
	v_cmp_ne_u32_e64 s[8:9], 34, v102
	v_cndmask_b32_e64 v87, v87, v246, s[0:1]
	v_cndmask_b32_e64 v67, v67, v246, s[4:5]
	v_cndmask_b32_e64 v88, v88, v246, s[8:9]
	v_med3_i32 v100, 34, v4, v5
	v_med3_i32 v101, 35, v98, v99
	v_med3_i32 v102, 35, v4, v5
	v_cmp_ne_u32_e64 s[0:1], 34, v100
	v_cmp_ne_u32_e64 s[4:5], 35, v101
	v_cmp_ne_u32_e64 s[8:9], 35, v102
	v_cndmask_b32_e64 v68, v68, v246, s[0:1]
	v_cndmask_b32_e64 v89, v89, v246, s[4:5]
	v_cndmask_b32_e64 v69, v69, v246, s[8:9]
	v_med3_i32 v100, 48, v98, v99
	v_med3_i32 v101, 48, v4, v5
	v_med3_i32 v102, 49, v98, v99
	v_cmp_ne_u32_e64 s[0:1], 48, v100
	v_cmp_ne_u32_e64 s[4:5], 48, v101
	v_cmp_ne_u32_e64 s[8:9], 49, v102
	v_cndmask_b32_e64 v82, v82, v246, s[0:1]
	v_cndmask_b32_e64 v78, v78, v246, s[4:5]
	v_cndmask_b32_e64 v83, v83, v246, s[8:9]
	v_med3_i32 v100, 49, v4, v5
	v_med3_i32 v101, 50, v98, v99
	v_med3_i32 v102, 50, v4, v5
	v_cmp_ne_u32_e64 s[0:1], 49, v100
	v_cmp_ne_u32_e64 s[4:5], 50, v101
	v_cmp_ne_u32_e64 s[8:9], 50, v102
	v_cndmask_b32_e64 v79, v79, v246, s[0:1]
	v_cndmask_b32_e64 v84, v84, v246, s[4:5]
	v_cndmask_b32_e64 v80, v80, v246, s[8:9]
	v_med3_i32 v100, 51, v98, v99
	v_med3_i32 v101, 51, v4, v5
	v_cmp_ne_u32_e64 s[0:1], 51, v100
	v_cmp_ne_u32_e64 s[4:5], 51, v101
	s_nop 1
	v_cndmask_b32_e64 v85, v85, v246, s[0:1]
	v_cndmask_b32_e64 v81, v81, v246, s[4:5]
	s_mov_b32 s25, 0xff800000
	s_mov_b32 s96, 0xff800000
; #define LAS __attribute__((address_space(3)))
; __device__ __forceinline__ u32x4 pack8m(const f32x4 v0, const f32x4 v1) { u32x4 w; w.x = cvtpk_m(v0[0], v0[1]); w.y = cvtpk_m(v0[2], v0[3]); w.z = cvtpk_m(v1[0], v1[1]); w.w = cvtpk_m(v1[2], v1[3]); return w; }
; __device__ __forceinline__ void attn_exp1(f32x4 (&s)[4], unsigned enm, bf16x8 (&pb)[2]) {
; #pragma unroll
;     for (int c = 0; c < 4; ++c)
; #pragma unroll
;         for (int i = 0; i < 4; ++i) s[c][i] = __builtin_amdgcn_exp2f(s[c][i]);
; #pragma unroll
;     for (int ks = 0; ks < 2; ++ks) { u32x4 pw = pack8m(s[2 * ks], s[2 * ks + 1]); pw.x &= enm; pw.y &= enm; pw.z &= enm; pw.w &= enm; pb[ks] = __builtin_bit_cast(bf16x8, pw); }
; }
; __device__ __forceinline__ void attn_pv1(LAS unsigned char* Vb, const bf16x8 (&pb)[2], int vlane, int swz, const bf16x8 onesf, AttnRow& st) {
; #pragma unroll
;     for (int ks = 0; ks < 2; ++ks) {
; #pragma unroll
;         for (int dt = 0; dt < 4; ++dt) {
;             LAS unsigned char* a0 = Vb + vlane + (2 * ks) * 2048 + ((dt ^ swz) * 32);
;             const bf16x8 vf = tr_frag(a0, a0 + 2048);
;             st.o[dt] = __builtin_amdgcn_mfma_f32_16x16x32_bf16(vf, pb[ks], st.o[dt], 0, 0, 0);
;         }
;         st.ol = __builtin_amdgcn_mfma_f32_16x16x32_bf16(onesf, pb[ks], st.ol, 0, 0, 0);
;     }
; }
; __device__ __forceinline__ void attn_step2x_nomax(LAS unsigned char* Vb, f32x4 (&s)[2][4], AttnRow (&st)[2], int kbase, int g4, const int (&lo)[2], const int (&hi)[2], const unsigned (&enm)[2], bool emask,
;                                                   int vlane, int swz, const bf16x8 onesf) {
;     ...
;     bf16x8 p0[2], p1[2];
;     attn_exp1(s[0], enm[0], p0);
;     attn_pv1(Vb, p0, vlane, swz, onesf, st[0]);
;     attn_exp1(s[1], enm[1], p1);
;     attn_pv1(Vb, p1, vlane, swz, onesf, st[1]);
.LBB0_2165:
	v_exp_f32_e32 v2, v94
	v_exp_f32_e32 v4, v95
	v_exp_f32_e32 v5, v96
	v_exp_f32_e32 v94, v97
	v_exp_f32_e32 v90, v90
	v_exp_f32_e32 v91, v91
	v_exp_f32_e32 v92, v92
	v_exp_f32_e32 v93, v93
	v_exp_f32_e32 v86, v86
	v_exp_f32_e32 v87, v87
	v_exp_f32_e32 v88, v88
	v_exp_f32_e32 v89, v89
	v_exp_f32_e32 v82, v82
	v_exp_f32_e32 v83, v83
	v_exp_f32_e32 v84, v84
	v_exp_f32_e32 v85, v85
	v_cvt_pk_bf16_f32 v102, v2, v4
	v_add_u32_e32 v2, s24, v218
	v_cvt_pk_bf16_f32 v103, v5, v94
	v_add_u32_e32 v109, v2, v221
	v_add_u32_e32 v5, v2, v222
	v_add_u32_e32 v4, v2, v223
	v_add_u32_e32 v2, v2, v224
	v_cvt_pk_bf16_f32 v104, v90, v91
	v_cvt_pk_bf16_f32 v105, v92, v93
	v_cvt_pk_bf16_f32 v98, v86, v87
	v_cvt_pk_bf16_f32 v99, v88, v89
	v_cvt_pk_bf16_f32 v100, v82, v83
	v_cvt_pk_bf16_f32 v101, v84, v85
	s_waitcnt vmcnt(0)
	ds_read_b64_tr_b16 v[90:91], v109 offset:32768
	ds_read_b64_tr_b16 v[92:93], v109 offset:34816
	ds_read_b64_tr_b16 v[94:95], v5 offset:32768
	ds_read_b64_tr_b16 v[96:97], v5 offset:34816
	ds_read_b64_tr_b16 v[86:87], v4 offset:32768
	ds_read_b64_tr_b16 v[88:89], v4 offset:34816
	ds_read_b64_tr_b16 v[82:83], v2 offset:32768
	ds_read_b64_tr_b16 v[84:85], v2 offset:34816
	s_waitcnt lgkmcnt(6)
	v_mfma_f32_16x16x32_bf16 v[58:61], v[90:93], v[102:105], v[58:61]
	v_exp_f32_e32 v74, v74
	v_exp_f32_e32 v75, v75
	v_exp_f32_e32 v76, v76
	s_waitcnt lgkmcnt(4)
	v_mfma_f32_16x16x32_bf16 v[54:57], v[94:97], v[102:105], v[54:57]
	v_exp_f32_e32 v77, v77
	v_exp_f32_e32 v70, v70
	v_exp_f32_e32 v71, v71
	s_waitcnt lgkmcnt(2)
	v_mfma_f32_16x16x32_bf16 v[46:49], v[86:89], v[102:105], v[46:49]
	v_exp_f32_e32 v72, v72
	v_exp_f32_e32 v73, v73
	v_exp_f32_e32 v78, v78
	s_waitcnt lgkmcnt(0)
	v_mfma_f32_16x16x32_bf16 v[50:53], v[82:85], v[102:105], v[50:53]
	v_exp_f32_e32 v79, v79
	v_exp_f32_e32 v80, v80
	v_exp_f32_e32 v81, v81
	v_mfma_f32_16x16x32_bf16 v[62:65], v[6:9], v[102:105], v[62:65]
	ds_read_b64_tr_b16 v[102:103], v109 offset:36864
	ds_read_b64_tr_b16 v[104:105], v109 offset:38912
	ds_read_b64_tr_b16 v[112:113], v5 offset:36864
	ds_read_b64_tr_b16 v[114:115], v5 offset:38912
	ds_read_b64_tr_b16 v[116:117], v4 offset:36864
	ds_read_b64_tr_b16 v[118:119], v4 offset:38912
	ds_read_b64_tr_b16 v[120:121], v2 offset:36864
	ds_read_b64_tr_b16 v[122:123], v2 offset:38912
	s_waitcnt lgkmcnt(6)
	v_mfma_f32_16x16x32_bf16 v[58:61], v[102:105], v[98:101], v[58:61]
	v_readlane_b32 s22, v251, 13
	s_cmp_ge_i32 s33, s22
	s_waitcnt lgkmcnt(4)
	v_mfma_f32_16x16x32_bf16 v[54:57], v[112:115], v[98:101], v[54:57]
	s_waitcnt lgkmcnt(2)
	v_mfma_f32_16x16x32_bf16 v[46:49], v[116:119], v[98:101], v[46:49]
	s_waitcnt lgkmcnt(0)
	v_mfma_f32_16x16x32_bf16 v[50:53], v[120:123], v[98:101], v[50:53]
	v_mfma_f32_16x16x32_bf16 v[62:65], v[6:9], v[98:101], v[62:65]
	v_exp_f32_e32 v98, v66
	v_exp_f32_e32 v99, v67
	v_exp_f32_e32 v100, v68
	v_exp_f32_e32 v101, v69
	v_cvt_pk_bf16_f32 v66, v74, v75
	v_cvt_pk_bf16_f32 v67, v76, v77
	v_cvt_pk_bf16_f32 v68, v70, v71
	v_cvt_pk_bf16_f32 v69, v72, v73
	v_cvt_pk_bf16_f32 v70, v98, v99
	v_cvt_pk_bf16_f32 v71, v100, v101
	v_mfma_f32_16x16x32_bf16 v[42:45], v[90:93], v[66:69], v[42:45]
	v_cvt_pk_bf16_f32 v72, v78, v79
	v_cvt_pk_bf16_f32 v73, v80, v81
	v_mfma_f32_16x16x32_bf16 v[34:37], v[94:97], v[66:69], v[34:37]
	v_mfma_f32_16x16x32_bf16 v[30:33], v[86:89], v[66:69], v[30:33]
	v_mfma_f32_16x16x32_bf16 v[26:29], v[82:85], v[66:69], v[26:29]
	v_mfma_f32_16x16x32_bf16 v[38:41], v[6:9], v[66:69], v[38:41]
	v_mfma_f32_16x16x32_bf16 v[42:45], v[102:105], v[70:73], v[42:45]
	v_mfma_f32_16x16x32_bf16 v[34:37], v[112:115], v[70:73], v[34:37]
	v_mfma_f32_16x16x32_bf16 v[30:33], v[116:119], v[70:73], v[30:33]
	v_mfma_f32_16x16x32_bf16 v[26:29], v[120:123], v[70:73], v[26:29]
	v_mfma_f32_16x16x32_bf16 v[38:41], v[6:9], v[70:73], v[38:41]
	s_cbranch_scc1 .LBB0_2171
; #define LAS __attribute__((address_space(3)))
; __device__ __forceinline__ void attn_qk2z(LAS unsigned char* Kb, const bf16x8 (&q)[2][2], int fr, int g4, f32x4 (&s)[2][4]) {
;     bf16x8 kf[4][2];
; #pragma unroll
;     for (int c = 0; c < 4; ++c)
; #pragma unroll
;         for (int ks = 0; ks < 2; ++ks) kf[c][ks] = *(const LAS bf16x8*)(Kb + pg8::lds_byte(16 * c + fr, 32 * ks + 8 * g4));
;     __builtin_amdgcn_sched_barrier(0);
; #pragma unroll
;     for (int c = 0; c < 4; ++c) {
; #pragma unroll
;         for (int ks = 0; ks < 2; ++ks) {
; #pragma unroll
;             for (int rb = 0; rb < 2; ++rb) s[rb][c] = __builtin_amdgcn_mfma_f32_16x16x32_bf16(kf[c][ks], q[rb][ks], ks == 0 ? (f32x4){0.f, 0.f, 0.f, 0.f} : s[rb][c], 0, 0, 0);
;         }
;     }
; }
; __device__ __forceinline__ void attn_step2x_nomax(LAS unsigned char* Vb, f32x4 (&s)[2][4], AttnRow (&st)[2], int kbase, int g4, const int (&lo)[2], const int (&hi)[2], const unsigned (&enm)[2], bool emask,
;                                                   int vlane, int swz, const bf16x8 onesf) {
;     if (emask) {
; #pragma unroll
;         for (int rb = 0; rb < 2; ++rb)
; #pragma unroll
;             for (int c = 0; c < 4; ++c)
; #pragma unroll
;                 for (int i = 0; i < 4; ++i) { const int key = kbase + 16 * c + 4 * g4 + i; if (key < lo[rb] || key > hi[rb]) s[rb][c][i] = -INFINITY; }
;     }
; __device__ __forceinline__ void ph_attn_fast2(const Args& a, LAS unsigned char* lds) {
;     ...
;                 AT_DMA(2, jt0, 0); if (nt_ > 1) AT_DMA(2, jt0 + 1, 1); __syncthreads();
	ds_read_b128 v[66:69], v110 offset:8192
	ds_read_b128 v[70:73], v110 offset:9216
	ds_read_b128 v[78:81], v110 offset:10240
	ds_read_b128 v[82:85], v110 offset:11264
	ds_read_b128 v[86:89], v110 offset:12288
	ds_read_b128 v[98:101], v110 offset:13312
	ds_read_b128 v[102:105], v110 offset:14336
	ds_read_b128 v[110:113], v110 offset:15360
	v_readlane_b32 s0, v251, 12
	s_cmp_eq_u32 s0, s33
	v_readlane_b32 s8, v251, 14
	s_cselect_b64 s[0:1], -1, 0
	s_add_i32 s4, s8, 64
	v_readlane_b32 s5, v251, 11
	s_cmp_lt_i32 s4, s5
	s_cselect_b64 s[4:5], -1, 0
	s_or_b64 s[0:1], s[0:1], s[4:5]
	s_waitcnt lgkmcnt(7)
	v_mfma_f32_16x16x32_bf16 v[74:77], v[66:69], v[10:13], 0
	s_andn2_b64 vcc, exec, s[0:1]
	v_readlane_b32 s25, v251, 8
	v_mfma_f32_16x16x32_bf16 v[66:69], v[66:69], v[18:21], 0
	s_waitcnt lgkmcnt(6)
	v_mfma_f32_16x16x32_bf16 v[94:97], v[70:73], v[14:17], v[74:77]
	v_mfma_f32_16x16x32_bf16 v[74:77], v[70:73], v[22:25], v[66:69]
	s_waitcnt lgkmcnt(5)
	v_mfma_f32_16x16x32_bf16 v[66:69], v[78:81], v[10:13], 0
	v_mfma_f32_16x16x32_bf16 v[70:73], v[78:81], v[18:21], 0
	s_waitcnt lgkmcnt(4)
	v_mfma_f32_16x16x32_bf16 v[90:93], v[82:85], v[14:17], v[66:69]
	s_waitcnt lgkmcnt(3)
	v_mfma_f32_16x16x32_bf16 v[66:69], v[86:89], v[10:13], 0
	v_mfma_f32_16x16x32_bf16 v[78:81], v[86:89], v[18:21], 0
	s_waitcnt lgkmcnt(2)
	v_mfma_f32_16x16x32_bf16 v[86:89], v[98:101], v[14:17], v[66:69]
	v_mfma_f32_16x16x32_bf16 v[66:69], v[98:101], v[22:25], v[78:81]
	s_waitcnt lgkmcnt(1)
	v_mfma_f32_16x16x32_bf16 v[78:81], v[102:105], v[10:13], 0
	v_mfma_f32_16x16x32_bf16 v[98:101], v[102:105], v[18:21], 0
	v_mfma_f32_16x16x32_bf16 v[70:73], v[82:85], v[22:25], v[70:73]
	s_waitcnt lgkmcnt(0)
	v_mfma_f32_16x16x32_bf16 v[82:85], v[110:113], v[14:17], v[78:81]
	v_mfma_f32_16x16x32_bf16 v[78:81], v[110:113], v[22:25], v[98:101]
	s_cbranch_vccnz .LBB0_2170
	s_nop 2
	v_add_u32_e32 v98, s8, v138
	v_add_u32_e32 v98, 64, v98
	v_sub_u32_e32 v99, v1, v98
	v_sub_u32_e32 v100, v106, v98
	v_sub_u32_e32 v101, v107, v98
	v_sub_u32_e32 v102, v108, v98
	v_med3_i32 v103, 0, v101, v102
	v_med3_i32 v104, 0, v99, v100
	v_med3_i32 v105, 1, v101, v102
	v_cmp_ne_u32_e64 s[0:1], 0, v103
	v_cmp_ne_u32_e64 s[4:5], 0, v104
	v_cmp_ne_u32_e64 s[8:9], 1, v105
	v_cndmask_b32_e64 v94, v94, v246, s[0:1]
	v_cndmask_b32_e64 v74, v74, v246, s[4:5]
	v_cndmask_b32_e64 v95, v95, v246, s[8:9]
	v_med3_i32 v103, 1, v99, v100
	v_med3_i32 v104, 2, v101, v102
	v_med3_i32 v105, 2, v99, v100
	v_cmp_ne_u32_e64 s[0:1], 1, v103
	v_cmp_ne_u32_e64 s[4:5], 2, v104
	v_cmp_ne_u32_e64 s[8:9], 2, v105
	v_cndmask_b32_e64 v75, v75, v246, s[0:1]
	v_cndmask_b32_e64 v96, v96, v246, s[4:5]
	v_cndmask_b32_e64 v76, v76, v246, s[8:9]
	v_med3_i32 v103, 3, v101, v102
	v_med3_i32 v104, 3, v99, v100
	v_med3_i32 v105, 16, v101, v102
	v_cmp_ne_u32_e64 s[0:1], 3, v103
	v_cmp_ne_u32_e64 s[4:5], 3, v104
	v_cmp_ne_u32_e64 s[8:9], 16, v105
	v_cndmask_b32_e64 v97, v97, v246, s[0:1]
	v_cndmask_b32_e64 v77, v77, v246, s[4:5]
	v_cndmask_b32_e64 v90, v90, v246, s[8:9]
	v_med3_i32 v103, 16, v99, v100
	v_med3_i32 v104, 17, v101, v102
	v_med3_i32 v105, 17, v99, v100
	v_cmp_ne_u32_e64 s[0:1], 16, v103
	v_cmp_ne_u32_e64 s[4:5], 17, v104
	v_cmp_ne_u32_e64 s[8:9], 17, v105
	v_cndmask_b32_e64 v70, v70, v246, s[0:1]
	v_cndmask_b32_e64 v91, v91, v246, s[4:5]
	v_cndmask_b32_e64 v71, v71, v246, s[8:9]
	v_med3_i32 v103, 18, v101, v102
	v_med3_i32 v104, 18, v99, v100
	v_med3_i32 v105, 19, v101, v102
	v_cmp_ne_u32_e64 s[0:1], 18, v103
	v_cmp_ne_u32_e64 s[4:5], 18, v104
	v_cmp_ne_u32_e64 s[8:9], 19, v105
	v_cndmask_b32_e64 v92, v92, v246, s[0:1]
	v_cndmask_b32_e64 v72, v72, v246, s[4:5]
	v_cndmask_b32_e64 v93, v93, v246, s[8:9]
	v_med3_i32 v103, 19, v99, v100
	v_med3_i32 v104, 32, v101, v102
	v_med3_i32 v105, 32, v99, v100
	v_cmp_ne_u32_e64 s[0:1], 19, v103
	v_cmp_ne_u32_e64 s[4:5], 32, v104
	v_cmp_ne_u32_e64 s[8:9], 32, v105
	v_cndmask_b32_e64 v73, v73, v246, s[0:1]
	v_cndmask_b32_e64 v86, v86, v246, s[4:5]
	v_cndmask_b32_e64 v66, v66, v246, s[8:9]
	v_med3_i32 v103, 33, v101, v102
	v_med3_i32 v104, 33, v99, v100
	v_med3_i32 v105, 34, v101, v102
	v_cmp_ne_u32_e64 s[0:1], 33, v103
	v_cmp_ne_u32_e64 s[4:5], 33, v104
	v_cmp_ne_u32_e64 s[8:9], 34, v105
	v_cndmask_b32_e64 v87, v87, v246, s[0:1]
	v_cndmask_b32_e64 v67, v67, v246, s[4:5]
	v_cndmask_b32_e64 v88, v88, v246, s[8:9]
	v_med3_i32 v103, 34, v99, v100
	v_med3_i32 v104, 35, v101, v102
	v_med3_i32 v105, 35, v99, v100
	v_cmp_ne_u32_e64 s[0:1], 34, v103
	v_cmp_ne_u32_e64 s[4:5], 35, v104
	v_cmp_ne_u32_e64 s[8:9], 35, v105
	v_cndmask_b32_e64 v68, v68, v246, s[0:1]
	v_cndmask_b32_e64 v89, v89, v246, s[4:5]
	v_cndmask_b32_e64 v69, v69, v246, s[8:9]
	v_med3_i32 v103, 48, v101, v102
	v_med3_i32 v104, 48, v99, v100
	v_med3_i32 v105, 49, v101, v102
	v_cmp_ne_u32_e64 s[0:1], 48, v103
	v_cmp_ne_u32_e64 s[4:5], 48, v104
	v_cmp_ne_u32_e64 s[8:9], 49, v105
	v_cndmask_b32_e64 v82, v82, v246, s[0:1]
	v_cndmask_b32_e64 v78, v78, v246, s[4:5]
	v_cndmask_b32_e64 v83, v83, v246, s[8:9]
	v_med3_i32 v103, 49, v99, v100
	v_med3_i32 v104, 50, v101, v102
	v_med3_i32 v105, 50, v99, v100
	v_cmp_ne_u32_e64 s[0:1], 49, v103
	v_cmp_ne_u32_e64 s[4:5], 50, v104
	v_cmp_ne_u32_e64 s[8:9], 50, v105
	v_cndmask_b32_e64 v79, v79, v246, s[0:1]
	v_cndmask_b32_e64 v84, v84, v246, s[4:5]
	v_cndmask_b32_e64 v80, v80, v246, s[8:9]
	v_med3_i32 v103, 51, v101, v102
	v_med3_i32 v104, 51, v99, v100
	v_cmp_ne_u32_e64 s[0:1], 51, v103
	v_cmp_ne_u32_e64 s[4:5], 51, v104
	s_nop 1
	v_cndmask_b32_e64 v85, v85, v246, s[0:1]
	v_cndmask_b32_e64 v81, v81, v246, s[4:5]
	s_mov_b32 s96, 0xff800000
